# O2: next head's LayerNorm gain/bias rows requested ahead of the epilogue stores; staging waits vmcnt(8) for them only
# speedup vs baseline: 1.0012x; 1.0012x over previous
; #define LAS __attribute__((address_space(3)))
; __device__ __forceinline__ void phase_sgu(CArgs a, LAS unsigned char* lds, int i2, int wv, int xw  ) {
;     ...
;             asm volatile("s_waitcnt vmcnt(0)" ::: "memory");
;             __syncthreads();
;             u32x2 uvp[4][4]; float bsp[4];
; #pragma unroll
;             for (int m = 0; m < 4; ++m) bsp[m] = a->in[I_SGUB][((size_t)i2 * 8 + h) * 128 + wr * 64 + m * 16 + fr];
; #pragma unroll
;             for (int m = 0; m < 4; ++m)
; #pragma unroll
;                 for (int n = 0; n < 4; ++n) uvp[m][n] = *(const u32x2*)(HB + (tok0 + wr * 64 + m * 16 + fr) * (2 * SGU_W) + h * 256 + wc * 64 + n * 16 + 4 * fq);
;             f32x4 acc[4][4];
; #pragma unroll
;             for (int m = 0; m < 4; ++m)
; #pragma unroll
;                 for (int n = 0; n < 4; ++n) acc[m][n] = (f32x4){0.f, 0.f, 0.f, 0.f};
; #pragma unroll
;             for (int ks = 0; ks < 4; ++ks) {
;                 bf16x8 bfr[4], af[4];
; #pragma unroll
;                 for (int m = 0; m < 4; ++m) { const int i = wr * 64 + m * 16 + fr; af[m] = *(const LAS bf16x8*)(wl + i * 256 + (((ks * 4 + fq) ^ (i & 15)) * 16)); }
; #pragma unroll
;                 for (int n = 0; n < 4; ++n) bfr[n] = *(const LAS bf16x8*)(vt + (wc * 64 + n * 16 + fr) * VS + ks * 32 + fq * 8);
; #pragma unroll
;                 for (int m = 0; m < 4; ++m)
; #pragma unroll
;                     for (int n = 0; n < 4; ++n) acc[m][n] = __builtin_amdgcn_mfma_f32_16x16x32_bf16(bfr[n], af[m], acc[m][n], 0, 0, 0);
.LBB0_283:
	s_waitcnt vmcnt(0)
	s_waitcnt lgkmcnt(0)
	s_barrier
	s_load_dwordx2 s[22:23], s[2:3], 0x88
	s_add_u32 s6, s6, 0x400
	s_addc_u32 s7, s7, 0
	v_lshl_add_u64 v[116:117], v[116:117], 0, s[60:61]
	v_lshl_add_u64 v[122:123], v[122:123], 0, s[60:61]
	s_waitcnt lgkmcnt(0)
	v_lshl_add_u64 v[32:33], s[22:23], 0, v[132:133]
	global_load_dword v168, v[32:33], off
	global_load_dword v156, v[32:33], off offset:64
	global_load_dword v144, v[32:33], off offset:128
	global_load_dword v134, v[32:33], off offset:192
	v_lshl_add_u64 v[32:33], s[4:5], 0, v[120:121]
	v_add_co_u32_e32 v34, vcc, s71, v32
	s_mov_b32 s22, 0x3a020000
	s_nop 0
	v_addc_co_u32_e32 v35, vcc, 0, v33, vcc
	global_load_dwordx2 v[174:175], v[34:35], off
	global_load_dwordx2 v[172:173], v[34:35], off offset:32
	global_load_dwordx2 v[170:171], v[34:35], off offset:64
	global_load_dwordx2 v[166:167], v[34:35], off offset:96
	v_add_co_u32_e32 v34, vcc, s22, v32
	s_mov_b32 s22, 0x3a040000
	s_nop 0
	v_addc_co_u32_e32 v35, vcc, 0, v33, vcc
	global_load_dwordx2 v[164:165], v[34:35], off
	global_load_dwordx2 v[162:163], v[34:35], off offset:32
	global_load_dwordx2 v[160:161], v[34:35], off offset:64
	global_load_dwordx2 v[158:159], v[34:35], off offset:96
	v_add_co_u32_e32 v34, vcc, s22, v32
	s_mov_b32 s22, 0x3a060000
	s_nop 0
	v_addc_co_u32_e32 v35, vcc, 0, v33, vcc
	v_add_co_u32_e32 v32, vcc, s22, v32
	global_load_dwordx2 v[154:155], v[34:35], off
	global_load_dwordx2 v[150:151], v[34:35], off offset:32
	global_load_dwordx2 v[148:149], v[34:35], off offset:64
	global_load_dwordx2 v[146:147], v[34:35], off offset:96
	v_addc_co_u32_e32 v33, vcc, 0, v33, vcc
	global_load_dwordx2 v[142:143], v[32:33], off
	global_load_dwordx2 v[140:141], v[32:33], off offset:32
	global_load_dwordx2 v[138:139], v[32:33], off offset:64
	global_load_dwordx2 v[136:137], v[32:33], off offset:96
	ds_read_b128 v[32:35], v196
	ds_read_b128 v[40:43], v196 offset:4096
	ds_read_b128 v[56:59], v196 offset:8192
	ds_read_b128 v[72:75], v196 offset:12288
	ds_read_b128 v[60:63], v197
	ds_read_b128 v[64:67], v197 offset:4352
	ds_read_b128 v[68:71], v197 offset:8704
	ds_read_b128 v[80:83], v197 offset:13056
	s_waitcnt lgkmcnt(3)
	v_mfma_f32_16x16x32_bf16 v[108:111], v[60:63], v[32:35], 0
	s_movk_i32 s22, 0xc0
	v_lshl_add_u64 v[120:121], v[120:121], 0, s[62:63]
	v_lshl_add_u64 v[124:125], v[124:125], 0, s[60:61]
	s_waitcnt lgkmcnt(2)
	v_mfma_f32_16x16x32_bf16 v[104:107], v[64:67], v[32:35], 0
	v_lshl_add_u64 v[126:127], v[126:127], 0, s[60:61]
	v_lshl_add_u64 v[128:129], v[128:129], 0, s[62:63]
	v_lshl_add_u64 v[130:131], v[130:131], 0, s[62:63]
	s_waitcnt lgkmcnt(1)
	v_mfma_f32_16x16x32_bf16 v[96:99], v[68:71], v[32:35], 0
	v_lshl_add_u64 v[132:133], v[132:133], 0, s[62:63]
	s_waitcnt lgkmcnt(0)
	v_mfma_f32_16x16x32_bf16 v[88:91], v[80:83], v[32:35], 0
	v_mfma_f32_16x16x32_bf16 v[76:79], v[60:63], v[40:43], 0
	v_mfma_f32_16x16x32_bf16 v[32:35], v[64:67], v[40:43], 0
	v_mfma_f32_16x16x32_bf16 v[36:39], v[68:71], v[40:43], 0
	v_mfma_f32_16x16x32_bf16 v[40:43], v[80:83], v[40:43], 0
	v_mfma_f32_16x16x32_bf16 v[44:47], v[60:63], v[56:59], 0
	v_mfma_f32_16x16x32_bf16 v[48:51], v[64:67], v[56:59], 0
	v_mfma_f32_16x16x32_bf16 v[52:55], v[68:71], v[56:59], 0
	v_mfma_f32_16x16x32_bf16 v[56:59], v[80:83], v[56:59], 0
	v_mfma_f32_16x16x32_bf16 v[60:63], v[60:63], v[72:75], 0
	v_mfma_f32_16x16x32_bf16 v[64:67], v[64:67], v[72:75], 0
	v_mfma_f32_16x16x32_bf16 v[68:71], v[68:71], v[72:75], 0
	v_mfma_f32_16x16x32_bf16 v[72:75], v[80:83], v[72:75], 0
	ds_read_b128 v[100:103], v198
	ds_read_b128 v[92:95], v198 offset:4096
	ds_read_b128 v[84:87], v198 offset:8192
	ds_read_b128 v[80:83], v198 offset:12288
	ds_read_b128 v[202:205], v197 offset:64
	ds_read_b128 v[206:209], v197 offset:4416
	ds_read_b128 v[210:213], v197 offset:8768
	ds_read_b128 v[214:217], v197 offset:13120
	s_waitcnt lgkmcnt(3)
	v_mfma_f32_16x16x32_bf16 v[108:111], v[202:205], v[100:103], v[108:111]
	s_waitcnt lgkmcnt(2)
	v_mfma_f32_16x16x32_bf16 v[104:107], v[206:209], v[100:103], v[104:107]
	s_waitcnt lgkmcnt(1)
	v_mfma_f32_16x16x32_bf16 v[96:99], v[210:213], v[100:103], v[96:99]
	s_waitcnt lgkmcnt(0)
	v_mfma_f32_16x16x32_bf16 v[88:91], v[214:217], v[100:103], v[88:91]
	v_mfma_f32_16x16x32_bf16 v[76:79], v[202:205], v[92:95], v[76:79]
	v_mfma_f32_16x16x32_bf16 v[32:35], v[206:209], v[92:95], v[32:35]
	v_mfma_f32_16x16x32_bf16 v[36:39], v[210:213], v[92:95], v[36:39]
	v_mfma_f32_16x16x32_bf16 v[40:43], v[214:217], v[92:95], v[40:43]
	v_mfma_f32_16x16x32_bf16 v[44:47], v[202:205], v[84:87], v[44:47]
	v_mfma_f32_16x16x32_bf16 v[48:51], v[206:209], v[84:87], v[48:51]
	v_mfma_f32_16x16x32_bf16 v[52:55], v[210:213], v[84:87], v[52:55]
	v_mfma_f32_16x16x32_bf16 v[56:59], v[214:217], v[84:87], v[56:59]
	v_mfma_f32_16x16x32_bf16 v[60:63], v[202:205], v[80:83], v[60:63]
	v_mfma_f32_16x16x32_bf16 v[64:67], v[206:209], v[80:83], v[64:67]
	v_mfma_f32_16x16x32_bf16 v[68:71], v[210:213], v[80:83], v[68:71]
	v_mfma_f32_16x16x32_bf16 v[72:75], v[214:217], v[80:83], v[72:75]
	ds_read_b128 v[80:83], v199
	ds_read_b128 v[84:87], v199 offset:4096
	ds_read_b128 v[92:95], v199 offset:8192
	ds_read_b128 v[100:103], v199 offset:12288
	ds_read_b128 v[202:205], v197 offset:128
	ds_read_b128 v[206:209], v197 offset:4480
	ds_read_b128 v[210:213], v197 offset:8832
	ds_read_b128 v[214:217], v197 offset:13184
	s_waitcnt lgkmcnt(3)
	v_mfma_f32_16x16x32_bf16 v[108:111], v[202:205], v[80:83], v[108:111]
	s_waitcnt lgkmcnt(2)
	v_mfma_f32_16x16x32_bf16 v[104:107], v[206:209], v[80:83], v[104:107]
	s_waitcnt lgkmcnt(1)
	v_mfma_f32_16x16x32_bf16 v[96:99], v[210:213], v[80:83], v[96:99]
	s_waitcnt lgkmcnt(0)
; #define LAS __attribute__((address_space(3)))
; __device__ __forceinline__ void phase_sgu(CArgs a, LAS unsigned char* lds, int i2, int wv, int xw  ) {
;     ...
;             for (int ks = 0; ks < 4; ++ks) {
;                 bf16x8 bfr[4], af[4];
; #pragma unroll
;                 for (int m = 0; m < 4; ++m) { const int i = wr * 64 + m * 16 + fr; af[m] = *(const LAS bf16x8*)(wl + i * 256 + (((ks * 4 + fq) ^ (i & 15)) * 16)); }
; #pragma unroll
;                 for (int n = 0; n < 4; ++n) bfr[n] = *(const LAS bf16x8*)(vt + (wc * 64 + n * 16 + fr) * VS + ks * 32 + fq * 8);
; #pragma unroll
;                 for (int m = 0; m < 4; ++m)
; #pragma unroll
;                     for (int n = 0; n < 4; ++n) acc[m][n] = __builtin_amdgcn_mfma_f32_16x16x32_bf16(bfr[n], af[m], acc[m][n], 0, 0, 0);
;             }
;             { int te = tz; asm volatile("" : "+v"(te));
;               const int le = te & 63, we = te >> 6, wr = we >> 2, wc = we & 3, fr = le & 15, fq = le >> 4;
; #pragma unroll
;             for (int m = 0; m < 4; ++m) { const int i = wr * 64 + m * 16 + fr; const float bs = bsp[m];
; #pragma unroll
;                 for (int n = 0; n < 4; ++n) { const int cc = h * 256 + wc * 64 + n * 16 + 4 * fq;
;                     const f32x4 sv = acc[m][n] + bs; const u32x2 uv = uvp[m][n];
;                     *(unsigned*)(YQ + (tok0 + i) * SGU_W + cc) = pk4_fp8(bflo(uv.x) * sv.x * QS_GATED, bfhi(uv.x) * sv.y * QS_GATED, bflo(uv.y) * sv.z * QS_GATED, bfhi(uv.y) * sv.w * QS_GATED); } } }
	v_mfma_f32_16x16x32_bf16 v[80:83], v[214:217], v[80:83], v[88:91]
	v_mfma_f32_16x16x32_bf16 v[76:79], v[202:205], v[84:87], v[76:79]
	v_mfma_f32_16x16x32_bf16 v[32:35], v[206:209], v[84:87], v[32:35]
	v_mfma_f32_16x16x32_bf16 v[36:39], v[210:213], v[84:87], v[36:39]
	v_mfma_f32_16x16x32_bf16 v[40:43], v[214:217], v[84:87], v[40:43]
	v_mfma_f32_16x16x32_bf16 v[44:47], v[202:205], v[92:95], v[44:47]
	v_mfma_f32_16x16x32_bf16 v[48:51], v[206:209], v[92:95], v[48:51]
	v_mfma_f32_16x16x32_bf16 v[52:55], v[210:213], v[92:95], v[52:55]
	v_mfma_f32_16x16x32_bf16 v[84:87], v[214:217], v[92:95], v[56:59]
	v_mfma_f32_16x16x32_bf16 v[88:91], v[202:205], v[100:103], v[60:63]
	v_mfma_f32_16x16x32_bf16 v[92:95], v[206:209], v[100:103], v[64:67]
	v_mfma_f32_16x16x32_bf16 v[202:205], v[210:213], v[100:103], v[68:71]
	v_mfma_f32_16x16x32_bf16 v[100:103], v[214:217], v[100:103], v[72:75]
	ds_read_b128 v[56:59], v200
	ds_read_b128 v[60:63], v200 offset:4096
	ds_read_b128 v[206:209], v200 offset:8192
	ds_read_b128 v[210:213], v200 offset:12288
	ds_read_b128 v[214:217], v197 offset:192
	ds_read_b128 v[218:221], v197 offset:4544
	ds_read_b128 v[222:225], v197 offset:8896
	ds_read_b128 v[226:229], v197 offset:13248
	s_waitcnt lgkmcnt(3)
	v_mfma_f32_16x16x32_bf16 v[108:111], v[214:217], v[56:59], v[108:111]
	s_waitcnt lgkmcnt(2)
	v_mfma_f32_16x16x32_bf16 v[104:107], v[218:221], v[56:59], v[104:107]
	s_waitcnt lgkmcnt(1)
	v_mfma_f32_16x16x32_bf16 v[96:99], v[222:225], v[56:59], v[96:99]
	s_waitcnt lgkmcnt(0)
	v_mfma_f32_16x16x32_bf16 v[80:83], v[226:229], v[56:59], v[80:83]
	v_mfma_f32_16x16x32_bf16 v[56:59], v[218:221], v[206:209], v[48:51]
	v_mfma_f32_16x16x32_bf16 v[48:51], v[226:229], v[206:209], v[84:87]
	s_waitcnt vmcnt(19)
	s_nop 4
	v_pk_add_f32 v[80:81], v[168:169], v[80:81] op_sel_hi:[0,1]
	v_pk_add_f32 v[82:83], v[168:169], v[82:83] op_sel_hi:[0,1]
	s_waitcnt vmcnt(17)
	v_pk_add_f32 v[56:57], v[144:145], v[56:57] op_sel_hi:[0,1]
	v_mov_b32_e32 v85, v112
	v_bfe_u32 v248, v112, 4, 2
	v_mov_b32_e32 v249, 0
	v_mul_u32_u24_e32 v248, 12, v248
	v_mfma_f32_16x16x32_bf16 v[76:79], v[214:217], v[60:63], v[76:79]
	v_and_b32_e32 v84, 15, v85
	v_ashrrev_i32_e32 v86, 2, v85
	v_and_or_b32 v84, v86, s39, v84
	v_lshrrev_b32_e32 v86, 2, v85
	v_and_b32_e32 v86, 12, v86
	v_and_or_b32 v85, v85, s22, v86
	v_add_u32_e32 v152, s24, v85
	v_ashrrev_i32_e32 v85, 31, v84
	v_mfma_f32_16x16x32_bf16 v[72:75], v[218:221], v[60:63], v[32:35]
	v_lshl_add_u64 v[86:87], s[20:21], 0, v[84:85]
	s_waitcnt vmcnt(15)
	v_lshlrev_b32_e32 v85, 16, v174
	v_lshlrev_b64 v[86:87], 11, v[86:87]
	v_mfma_f32_16x16x32_bf16 v[68:71], v[222:225], v[60:63], v[36:39]
	v_lshl_add_u64 v[86:87], s[10:11], 0, v[86:87]
	v_lshl_add_u64 v[86:87], v[86:87], 0, v[152:153]
	v_pk_add_f32 v[76:77], v[156:157], v[76:77] op_sel_hi:[0,1]
	v_mfma_f32_16x16x32_bf16 v[64:67], v[226:229], v[60:63], v[40:43]
	v_add_f32_e64 v78, v156, v78
	v_add_f32_e64 v79, v156, v79
	v_pk_add_f32 v[72:73], v[156:157], v[72:73] op_sel_hi:[0,1]
	v_pk_add_f32 v[74:75], v[156:157], v[74:75] op_sel_hi:[0,1]
	v_mfma_f32_16x16x32_bf16 v[60:63], v[214:217], v[206:209], v[44:47]
	v_add_f32_e64 v68, v156, v68
	v_add_f32_e64 v69, v156, v69
	v_pk_add_f32 v[70:71], v[156:157], v[70:71] op_sel_hi:[0,1]
	v_pk_add_f32 v[64:65], v[156:157], v[64:65] op_sel_hi:[0,1]
	v_mfma_f32_16x16x32_bf16 v[44:47], v[214:217], v[210:213], v[88:91]
	v_add_f32_e64 v66, v156, v66
	v_add_f32_e64 v67, v156, v67
	s_nop 0
	v_pk_add_f32 v[60:61], v[144:145], v[60:61] op_sel_hi:[0,1]
	v_pk_add_f32 v[62:63], v[144:145], v[62:63] op_sel_hi:[0,1]
	v_pk_add_f32 v[90:91], v[168:169], v[108:109] op_sel_hi:[0,1]
	v_mul_f32_e32 v85, v90, v85
	v_and_b32_e32 v90, 0xffff0000, v174
	v_pk_add_f32 v[88:89], v[168:169], v[110:111] op_sel_hi:[0,1]
	v_mul_f32_e32 v90, v91, v90
	v_lshlrev_b32_e32 v91, 16, v175
	v_mul_f32_e32 v85, 0x41000000, v85
	v_mul_f32_e32 v90, 0x41000000, v90
	v_mul_f32_e32 v88, v88, v91
	v_and_b32_e32 v91, 0xffff0000, v175
	v_mul_f32_e32 v89, v89, v91
	v_med3_f32 v85, v85, s51, v187
	v_med3_f32 v90, v90, s51, v187
	v_cvt_pk_fp8_f32 v232, v85, v90
	v_mul_f32_e32 v88, 0x41000000, v88
	v_mul_f32_e32 v89, 0x41000000, v89
	v_med3_f32 v88, v88, s51, v187
	v_med3_f32 v89, v89, s51, v187
	v_cvt_pk_fp8_f32 v232, v88, v89 op_sel:[0,0,1]
	s_waitcnt vmcnt(14)
	v_lshlrev_b32_e32 v85, 16, v172
	v_pk_add_f32 v[88:89], v[168:169], v[106:107] op_sel_hi:[0,1]
	v_mfma_f32_16x16x32_bf16 v[52:55], v[222:225], v[206:209], v[52:55]
	v_pk_add_f32 v[90:91], v[168:169], v[104:105] op_sel_hi:[0,1]
	v_mul_f32_e32 v85, v90, v85
	v_and_b32_e32 v90, 0xffff0000, v172
	v_mul_f32_e32 v90, v91, v90
	v_lshlrev_b32_e32 v91, 16, v173
	v_mul_f32_e32 v85, 0x41000000, v85
	v_mul_f32_e32 v90, 0x41000000, v90
	v_mul_f32_e32 v88, v88, v91
	v_and_b32_e32 v91, 0xffff0000, v173
	v_mul_f32_e32 v89, v89, v91
	v_med3_f32 v85, v85, s51, v187
	v_med3_f32 v90, v90, s51, v187
	v_cvt_pk_fp8_f32 v233, v85, v90
	v_mul_f32_e32 v88, 0x41000000, v88
	v_mul_f32_e32 v89, 0x41000000, v89
	v_med3_f32 v88, v88, s51, v187
	v_med3_f32 v89, v89, s51, v187
	v_cvt_pk_fp8_f32 v233, v88, v89 op_sel:[0,0,1]
	s_waitcnt vmcnt(13)
	v_lshlrev_b32_e32 v85, 16, v170
	v_pk_add_f32 v[88:89], v[168:169], v[98:99] op_sel_hi:[0,1]
	v_pk_add_f32 v[58:59], v[144:145], v[58:59] op_sel_hi:[0,1]
	v_pk_add_f32 v[90:91], v[168:169], v[96:97] op_sel_hi:[0,1]
	v_mul_f32_e32 v85, v90, v85
	v_and_b32_e32 v90, 0xffff0000, v170
	v_mul_f32_e32 v90, v91, v90
	v_lshlrev_b32_e32 v91, 16, v171
	v_mul_f32_e32 v85, 0x41000000, v85
	v_mul_f32_e32 v90, 0x41000000, v90
	v_mul_f32_e32 v88, v88, v91
	v_and_b32_e32 v91, 0xffff0000, v171
	v_mul_f32_e32 v89, v89, v91
	v_med3_f32 v85, v85, s51, v187
	v_med3_f32 v90, v90, s51, v187
	v_cvt_pk_fp8_f32 v234, v85, v90
	s_waitcnt vmcnt(12)
; __device__ __forceinline__ void phase_sgu(CArgs a, LAS unsigned char* lds, int i2, int wv, int xw  ) {
;     ...
;             for (int m = 0; m < 4; ++m) { const int i = wr * 64 + m * 16 + fr; const float bs = bsp[m];
; #pragma unroll
;                 for (int n = 0; n < 4; ++n) { const int cc = h * 256 + wc * 64 + n * 16 + 4 * fq;
;                     const f32x4 sv = acc[m][n] + bs; const u32x2 uv = uvp[m][n];
;                     *(unsigned*)(YQ + (tok0 + i) * SGU_W + cc) = pk4_fp8(bflo(uv.x) * sv.x * QS_GATED, bfhi(uv.x) * sv.y * QS_GATED, bflo(uv.y) * sv.z * QS_GATED, bfhi(uv.y) * sv.w * QS_GATED); } } }
	v_lshlrev_b32_e32 v85, 16, v166
	v_mul_f32_e32 v80, v80, v85
	v_and_b32_e32 v85, 0xffff0000, v166
	v_mul_f32_e32 v81, v81, v85
	v_lshlrev_b32_e32 v85, 16, v167
	v_mul_f32_e32 v80, 0x41000000, v80
	v_mul_f32_e32 v81, 0x41000000, v81
	v_mul_f32_e32 v82, v82, v85
	v_and_b32_e32 v85, 0xffff0000, v167
	v_mul_f32_e32 v83, v83, v85
	v_med3_f32 v80, v80, s51, v187
	v_med3_f32 v81, v81, s51, v187
	v_cvt_pk_fp8_f32 v235, v80, v81
	v_mul_f32_e32 v82, 0x41000000, v82
	v_mul_f32_e32 v83, 0x41000000, v83
	v_med3_f32 v82, v82, s51, v187
	v_med3_f32 v83, v83, s51, v187
	v_cvt_pk_fp8_f32 v235, v82, v83 op_sel:[0,0,1]
	s_waitcnt vmcnt(11)
	v_lshlrev_b32_e32 v82, 16, v164
	v_mul_f32_e32 v76, v76, v82
	v_and_b32_e32 v82, 0xffff0000, v164
	v_mul_f32_e32 v77, v77, v82
	v_lshlrev_b32_e32 v82, 16, v165
	v_mul_f32_e32 v76, 0x41000000, v76
	v_mul_f32_e32 v77, 0x41000000, v77
	v_mul_f32_e32 v78, v78, v82
	v_and_b32_e32 v82, 0xffff0000, v165
	v_mul_f32_e32 v79, v79, v82
	v_med3_f32 v76, v76, s51, v187
	v_med3_f32 v77, v77, s51, v187
	v_cvt_pk_fp8_f32 v236, v76, v77
	v_mul_f32_e32 v78, 0x41000000, v78
	v_mul_f32_e32 v79, 0x41000000, v79
	v_med3_f32 v78, v78, s51, v187
	v_med3_f32 v79, v79, s51, v187
	v_cvt_pk_fp8_f32 v236, v78, v79 op_sel:[0,0,1]
	s_waitcnt vmcnt(10)
	v_lshlrev_b32_e32 v78, 16, v162
	v_mul_f32_e32 v72, v72, v78
	v_and_b32_e32 v78, 0xffff0000, v162
	v_mul_f32_e32 v73, v73, v78
	v_lshlrev_b32_e32 v78, 16, v163
	v_mul_f32_e32 v72, 0x41000000, v72
	v_mul_f32_e32 v73, 0x41000000, v73
	v_mul_f32_e32 v74, v74, v78
	v_and_b32_e32 v78, 0xffff0000, v163
	v_mul_f32_e32 v75, v75, v78
	v_med3_f32 v72, v72, s51, v187
	v_med3_f32 v73, v73, s51, v187
	v_cvt_pk_fp8_f32 v237, v72, v73
	s_waitcnt vmcnt(9)
	v_lshlrev_b32_e32 v72, 16, v160
	v_mul_f32_e32 v68, v68, v72
	v_and_b32_e32 v72, 0xffff0000, v160
	v_mul_f32_e32 v69, v69, v72
	v_lshlrev_b32_e32 v72, 16, v161
	v_mul_f32_e32 v68, 0x41000000, v68
	v_mul_f32_e32 v69, 0x41000000, v69
	v_mul_f32_e32 v70, v70, v72
	v_and_b32_e32 v72, 0xffff0000, v161
	v_mul_f32_e32 v71, v71, v72
	v_med3_f32 v68, v68, s51, v187
	v_med3_f32 v69, v69, s51, v187
	v_cvt_pk_fp8_f32 v238, v68, v69
	s_waitcnt vmcnt(8)
	v_lshlrev_b32_e32 v68, 16, v158
	v_mul_f32_e32 v64, v64, v68
	v_and_b32_e32 v68, 0xffff0000, v158
	v_mul_f32_e32 v65, v65, v68
	v_lshlrev_b32_e32 v68, 16, v159
	v_mul_f32_e32 v64, 0x41000000, v64
	v_mul_f32_e32 v65, 0x41000000, v65
	v_mul_f32_e32 v66, v66, v68
	v_and_b32_e32 v68, 0xffff0000, v159
	v_mul_f32_e32 v67, v67, v68
	v_med3_f32 v64, v64, s51, v187
	v_med3_f32 v65, v65, s51, v187
	v_cvt_pk_fp8_f32 v239, v64, v65
	v_mul_f32_e32 v66, 0x41000000, v66
	v_mul_f32_e32 v67, 0x41000000, v67
	v_med3_f32 v66, v66, s51, v187
	v_med3_f32 v67, v67, s51, v187
	v_cvt_pk_fp8_f32 v239, v66, v67 op_sel:[0,0,1]
	s_waitcnt vmcnt(7)
	v_lshlrev_b32_e32 v66, 16, v154
	v_mul_f32_e32 v60, v60, v66
	v_and_b32_e32 v66, 0xffff0000, v154
	v_mul_f32_e32 v61, v61, v66
	v_lshlrev_b32_e32 v66, 16, v155
	v_mul_f32_e32 v60, 0x41000000, v60
	v_mul_f32_e32 v61, 0x41000000, v61
	v_mul_f32_e32 v62, v62, v66
	v_and_b32_e32 v66, 0xffff0000, v155
	v_mul_f32_e32 v63, v63, v66
	v_med3_f32 v60, v60, s51, v187
	v_med3_f32 v61, v61, s51, v187
	v_cvt_pk_fp8_f32 v240, v60, v61
	v_mul_f32_e32 v62, 0x41000000, v62
	v_mul_f32_e32 v63, 0x41000000, v63
	v_med3_f32 v62, v62, s51, v187
	v_med3_f32 v63, v63, s51, v187
	v_cvt_pk_fp8_f32 v240, v62, v63 op_sel:[0,0,1]
	s_waitcnt vmcnt(6)
	v_lshlrev_b32_e32 v62, 16, v150
	v_mul_f32_e32 v56, v56, v62
	v_and_b32_e32 v62, 0xffff0000, v150
	v_mul_f32_e32 v57, v57, v62
	v_lshlrev_b32_e32 v62, 16, v151
	v_mul_f32_e32 v56, 0x41000000, v56
	v_mul_f32_e32 v57, 0x41000000, v57
	v_mul_f32_e32 v58, v58, v62
	v_and_b32_e32 v62, 0xffff0000, v151
	v_mul_f32_e32 v59, v59, v62
	v_med3_f32 v56, v56, s51, v187
	v_med3_f32 v57, v57, s51, v187
	v_cvt_pk_fp8_f32 v241, v56, v57
	v_pk_add_f32 v[52:53], v[144:145], v[52:53] op_sel_hi:[0,1]
	s_waitcnt vmcnt(5)
	v_lshlrev_b32_e32 v56, 16, v148
	v_mul_f32_e32 v52, v52, v56
	v_and_b32_e32 v56, 0xffff0000, v148
	v_pk_add_f32 v[54:55], v[144:145], v[54:55] op_sel_hi:[0,1]
	v_mul_f32_e32 v53, v53, v56
	v_lshlrev_b32_e32 v56, 16, v149
	v_mul_f32_e32 v52, 0x41000000, v52
	v_mul_f32_e32 v53, 0x41000000, v53
	v_mul_f32_e32 v54, v54, v56
	v_and_b32_e32 v56, 0xffff0000, v149
	v_mul_f32_e32 v55, v55, v56
	v_med3_f32 v52, v52, s51, v187
	v_med3_f32 v53, v53, s51, v187
	v_cvt_pk_fp8_f32 v242, v52, v53
	v_pk_add_f32 v[48:49], v[144:145], v[48:49] op_sel_hi:[0,1]
	s_waitcnt vmcnt(4)
	v_lshlrev_b32_e32 v52, 16, v146
	v_mul_f32_e32 v48, v48, v52
	v_and_b32_e32 v52, 0xffff0000, v146
	v_pk_add_f32 v[50:51], v[144:145], v[50:51] op_sel_hi:[0,1]
	v_mul_f32_e32 v49, v49, v52
	v_lshlrev_b32_e32 v52, 16, v147
	v_mul_f32_e32 v48, 0x41000000, v48
	v_mul_f32_e32 v49, 0x41000000, v49
	v_mul_f32_e32 v50, v50, v52
	v_and_b32_e32 v52, 0xffff0000, v147
	v_mul_f32_e32 v51, v51, v52
	v_med3_f32 v48, v48, s51, v187
	v_med3_f32 v49, v49, s51, v187
	v_cvt_pk_fp8_f32 v243, v48, v49
	v_mul_f32_e32 v50, 0x41000000, v50
	v_mul_f32_e32 v51, 0x41000000, v51
	v_med3_f32 v50, v50, s51, v187
	v_med3_f32 v51, v51, s51, v187
	v_cvt_pk_fp8_f32 v243, v50, v51 op_sel:[0,0,1]
	v_pk_add_f32 v[44:45], v[134:135], v[44:45] op_sel_hi:[0,1]
	s_waitcnt vmcnt(3)
; __device__ __forceinline__ void phase_sgu(CArgs a, LAS unsigned char* lds, int i2, int wv, int xw  ) {
;     ...
;                 for (int q = 0; q < 2; ++q) { const float* gp = lg + h * 256 + (cA + 16 * q) * 8; const float* bp = lb + h * 256 + (cA + 16 * q) * 8;
;                     gg[q][0] = *(const f32x4*)gp; gg[q][1] = *(const f32x4*)(gp + 4); bb[q][0] = *(const f32x4*)bp; bb[q][1] = *(const f32x4*)(bp + 4); }
;     ...
;             { int te = tz; asm volatile("" : "+v"(te));
;               const int le = te & 63, we = te >> 6, wr = we >> 2, wc = we & 3, fr = le & 15, fq = le >> 4;
; #pragma unroll
;             for (int m = 0; m < 4; ++m) { const int i = wr * 64 + m * 16 + fr; const float bs = bsp[m];
; #pragma unroll
;                 for (int n = 0; n < 4; ++n) { const int cc = h * 256 + wc * 64 + n * 16 + 4 * fq;
;                     const f32x4 sv = acc[m][n] + bs; const u32x2 uv = uvp[m][n];
;                     *(unsigned*)(YQ + (tok0 + i) * SGU_W + cc) = pk4_fp8(bflo(uv.x) * sv.x * QS_GATED, bfhi(uv.x) * sv.y * QS_GATED, bflo(uv.y) * sv.z * QS_GATED, bfhi(uv.y) * sv.w * QS_GATED); } } }
	v_lshlrev_b32_e32 v50, 16, v142
	v_mul_f32_e32 v44, v44, v50
	v_and_b32_e32 v50, 0xffff0000, v142
	v_pk_add_f32 v[46:47], v[134:135], v[46:47] op_sel_hi:[0,1]
	v_mul_f32_e32 v45, v45, v50
	v_lshlrev_b32_e32 v50, 16, v143
	v_mul_f32_e32 v44, 0x41000000, v44
	v_mul_f32_e32 v45, 0x41000000, v45
	v_mul_f32_e32 v46, v46, v50
	v_and_b32_e32 v50, 0xffff0000, v143
	v_mul_f32_e32 v47, v47, v50
	v_med3_f32 v44, v44, s51, v187
	v_med3_f32 v45, v45, s51, v187
	v_mfma_f32_16x16x32_bf16 v[40:43], v[218:221], v[210:213], v[92:95]
	v_cvt_pk_fp8_f32 v244, v44, v45
	v_mul_f32_e32 v46, 0x41000000, v46
	v_mul_f32_e32 v47, 0x41000000, v47
	v_med3_f32 v46, v46, s51, v187
	v_med3_f32 v47, v47, s51, v187
	v_cvt_pk_fp8_f32 v244, v46, v47 op_sel:[0,0,1]
	s_nop 1
	v_pk_add_f32 v[40:41], v[134:135], v[40:41] op_sel_hi:[0,1]
	s_waitcnt vmcnt(2)
	v_lshlrev_b32_e32 v46, 16, v140
	v_mfma_f32_16x16x32_bf16 v[36:39], v[222:225], v[210:213], v[202:205]
	v_mul_f32_e32 v40, v40, v46
	v_and_b32_e32 v46, 0xffff0000, v140
	v_pk_add_f32 v[42:43], v[134:135], v[42:43] op_sel_hi:[0,1]
	v_mul_f32_e32 v41, v41, v46
	v_lshlrev_b32_e32 v46, 16, v141
	v_mul_f32_e32 v40, 0x41000000, v40
	v_mul_f32_e32 v41, 0x41000000, v41
	v_mul_f32_e32 v42, v42, v46
	v_and_b32_e32 v46, 0xffff0000, v141
	v_mul_f32_e32 v43, v43, v46
	v_med3_f32 v40, v40, s51, v187
	v_med3_f32 v41, v41, s51, v187
	v_cvt_pk_fp8_f32 v245, v40, v41
	v_pk_add_f32 v[36:37], v[134:135], v[36:37] op_sel_hi:[0,1]
	s_waitcnt vmcnt(1)
	v_lshlrev_b32_e32 v40, 16, v138
	v_mfma_f32_16x16x32_bf16 v[32:35], v[226:229], v[210:213], v[100:103]
	v_mul_f32_e32 v36, v36, v40
	v_and_b32_e32 v40, 0xffff0000, v138
	v_pk_add_f32 v[38:39], v[134:135], v[38:39] op_sel_hi:[0,1]
	v_mul_f32_e32 v37, v37, v40
	v_lshlrev_b32_e32 v40, 16, v139
	v_mul_f32_e32 v36, 0x41000000, v36
	v_mul_f32_e32 v37, 0x41000000, v37
	v_mul_f32_e32 v38, v38, v40
	v_and_b32_e32 v40, 0xffff0000, v139
	v_mul_f32_e32 v39, v39, v40
	v_med3_f32 v36, v36, s51, v187
	v_med3_f32 v37, v37, s51, v187
	v_cvt_pk_fp8_f32 v246, v36, v37
	v_pk_add_f32 v[32:33], v[134:135], v[32:33] op_sel_hi:[0,1]
	s_waitcnt vmcnt(0)
	v_lshlrev_b32_e32 v36, 16, v136
	v_mul_f32_e32 v32, v32, v36
	v_and_b32_e32 v36, 0xffff0000, v136
	v_pk_add_f32 v[34:35], v[134:135], v[34:35] op_sel_hi:[0,1]
	v_mul_f32_e32 v33, v33, v36
	v_lshlrev_b32_e32 v36, 16, v137
	v_mul_f32_e32 v32, 0x41000000, v32
	v_mul_f32_e32 v33, 0x41000000, v33
	v_mul_f32_e32 v34, v34, v36
	v_and_b32_e32 v36, 0xffff0000, v137
	v_mul_f32_e32 v35, v35, v36
	v_med3_f32 v32, v32, s51, v187
	v_med3_f32 v33, v33, s51, v187
	v_cvt_pk_fp8_f32 v247, v32, v33
	v_mul_f32_e32 v88, 0x41000000, v88
	v_mul_f32_e32 v89, 0x41000000, v89
	v_or_b32_e32 v80, 16, v84
	v_mul_f32_e32 v74, 0x41000000, v74
	v_mul_f32_e32 v75, 0x41000000, v75
	v_mul_f32_e32 v70, 0x41000000, v70
	v_mul_f32_e32 v71, 0x41000000, v71
	v_or_b32_e32 v64, 32, v84
	v_mul_f32_e32 v58, 0x41000000, v58
	v_mul_f32_e32 v59, 0x41000000, v59
	v_mul_f32_e32 v54, 0x41000000, v54
	v_mul_f32_e32 v55, 0x41000000, v55
	v_or_b32_e32 v48, 48, v84
	v_mul_f32_e32 v42, 0x41000000, v42
	v_mul_f32_e32 v43, 0x41000000, v43
	v_mul_f32_e32 v38, 0x41000000, v38
	v_mul_f32_e32 v39, 0x41000000, v39
	v_mul_f32_e32 v34, 0x41000000, v34
	v_mul_f32_e32 v35, 0x41000000, v35
	v_med3_f32 v88, v88, s51, v187
	v_med3_f32 v89, v89, s51, v187
	v_ashrrev_i32_e32 v81, 31, v80
	v_med3_f32 v74, v74, s51, v187
	v_med3_f32 v75, v75, s51, v187
	v_med3_f32 v70, v70, s51, v187
	v_med3_f32 v71, v71, s51, v187
	v_ashrrev_i32_e32 v65, 31, v64
	v_med3_f32 v58, v58, s51, v187
	v_med3_f32 v59, v59, s51, v187
	v_med3_f32 v54, v54, s51, v187
	v_med3_f32 v55, v55, s51, v187
	v_ashrrev_i32_e32 v49, 31, v48
	v_med3_f32 v42, v42, s51, v187
	v_med3_f32 v43, v43, s51, v187
	v_med3_f32 v38, v38, s51, v187
	v_med3_f32 v39, v39, s51, v187
	v_med3_f32 v34, v34, s51, v187
	v_med3_f32 v35, v35, s51, v187
	v_cvt_pk_fp8_f32 v234, v88, v89 op_sel:[0,0,1]
	v_lshl_add_u64 v[80:81], s[20:21], 0, v[80:81]
	v_cvt_pk_fp8_f32 v237, v74, v75 op_sel:[0,0,1]
	v_cvt_pk_fp8_f32 v238, v70, v71 op_sel:[0,0,1]
	v_lshl_add_u64 v[64:65], s[20:21], 0, v[64:65]
	v_cvt_pk_fp8_f32 v241, v58, v59 op_sel:[0,0,1]
	v_cvt_pk_fp8_f32 v242, v54, v55 op_sel:[0,0,1]
	v_lshl_add_u64 v[48:49], s[20:21], 0, v[48:49]
	v_cvt_pk_fp8_f32 v245, v42, v43 op_sel:[0,0,1]
	v_cvt_pk_fp8_f32 v246, v38, v39 op_sel:[0,0,1]
	v_cvt_pk_fp8_f32 v247, v34, v35 op_sel:[0,0,1]
	v_lshlrev_b64 v[80:81], 11, v[80:81]
	v_lshlrev_b64 v[64:65], 11, v[64:65]
	v_lshlrev_b64 v[48:49], 11, v[48:49]
	v_lshl_add_u64 v[80:81], s[10:11], 0, v[80:81]
	v_lshl_add_u64 v[64:65], s[10:11], 0, v[64:65]
	v_lshl_add_u64 v[48:49], s[10:11], 0, v[48:49]
	s_addk_i32 s24, 0x100
	v_lshl_add_u64 v[76:77], v[80:81], 0, v[152:153]
	v_lshl_add_u64 v[60:61], v[64:65], 0, v[152:153]
	v_lshl_add_u64 v[44:45], v[48:49], 0, v[152:153]
	s_cmpk_eq_i32 s6, 0x1000
	v_permlane16_swap_b32_e32 v232, v233
	v_permlane16_swap_b32_e32 v234, v235
	v_permlane16_swap_b32_e32 v236, v237
	v_permlane16_swap_b32_e32 v238, v239
	v_permlane16_swap_b32_e32 v240, v241
	v_permlane16_swap_b32_e32 v242, v243
	v_permlane16_swap_b32_e32 v244, v245
	v_permlane16_swap_b32_e32 v246, v247
	v_lshl_add_u64 v[178:179], v[86:87], 0, v[248:249]
	v_lshl_add_u64 v[180:181], v[76:77], 0, v[248:249]
	v_lshl_add_u64 v[230:231], v[60:61], 0, v[248:249]
	v_lshl_add_u64 v[250:251], v[44:45], 0, v[248:249]
	s_cbranch_scc1 .Lo2_nopf
	v_lshl_add_u64 v[36:37], v[118:119], 0, s[6:7]
	v_lshl_add_u64 v[44:45], v[114:115], 0, s[6:7]
	global_load_dwordx4 v[48:51], v[36:37], off offset:16
	global_load_dwordx4 v[56:59], v[36:37], off
	global_load_dwordx4 v[52:55], v[44:45], off offset:16
	global_load_dwordx4 v[60:63], v[44:45], off
	global_load_dwordx4 v[32:35], v[36:37], off offset:528
	global_load_dwordx4 v[40:43], v[36:37], off offset:512
	global_load_dwordx4 v[36:39], v[44:45], off offset:528
	global_load_dwordx4 v[44:47], v[44:45], off offset:512
; #define LAS __attribute__((address_space(3)))
; __device__ __forceinline__ void phase_sgu(CArgs a, LAS unsigned char* lds, int i2, int wv, int xw  ) {
;     ...
;             for (int q = 0; q < 4; ++q) { const int r = 4 * (8 * q + wave) + (lane >> 4);
;                 __builtin_amdgcn_global_load_lds((const unsigned*)(wm + (size_t)r * 128 + 8 * ((lane & 15) ^ (r & 15))), (LAS unsigned*)(wl + (8 * q + wave) * 1024), 16, 0, 0); }
;             {
;                 const int cA = 2 * wave + (lane >> 5);
;                 f32x4 gg[2][2], bb[2][2];
; #pragma unroll
;                 for (int q = 0; q < 2; ++q) { const float* gp = lg + h * 256 + (cA + 16 * q) * 8; const float* bp = lb + h * 256 + (cA + 16 * q) * 8;
;                     gg[q][0] = *(const f32x4*)gp; gg[q][1] = *(const f32x4*)(gp + 4); bb[q][0] = *(const f32x4*)bp; bb[q][1] = *(const f32x4*)(bp + 4); }
; #pragma unroll
;                 for (int it = 0; it < 8; ++it) { const int j = 32 * (it & 3) + (lane & 31), q = it >> 2, c8 = cA + 16 * q;
;                     const float m = mu[j], r = rs[j]; const u32x4 raw = vraw[it];
.Lo2_nopf:
	v_permlane32_swap_b32_e32 v232, v234
	v_permlane32_swap_b32_e32 v233, v235
	v_permlane32_swap_b32_e32 v236, v238
	v_permlane32_swap_b32_e32 v237, v239
	v_permlane32_swap_b32_e32 v240, v242
	v_permlane32_swap_b32_e32 v241, v243
	v_permlane32_swap_b32_e32 v244, v246
	v_permlane32_swap_b32_e32 v245, v247
	s_nop 1
	global_store_dwordx4 v[178:179], v[232:235], off
	global_store_dwordx4 v[180:181], v[236:239], off
	global_store_dwordx4 v[230:231], v[240:243], off
	global_store_dwordx4 v[250:251], v[244:247], off
	s_barrier
	s_cbranch_scc1 .LBB0_279
	s_add_i32 s22, 0, 0x12000
	v_lshl_add_u64 v[230:231], s[4:5], 0, v[116:117]
	s_add_i32 m0, s22, s25
	s_nop 0
	global_load_lds_dwordx4 v[230:231], off
	v_lshl_add_u64 v[230:231], s[4:5], 0, v[122:123]
	s_add_i32 m0, s22, s28
	s_nop 0
	global_load_lds_dwordx4 v[230:231], off
	v_lshl_add_u64 v[230:231], s[4:5], 0, v[124:125]
	s_add_i32 m0, s22, s33
	v_lshlrev_b32_e32 v66, 16, v0
	global_load_lds_dwordx4 v[230:231], off
	v_lshl_add_u64 v[230:231], s[4:5], 0, v[126:127]
	s_add_i32 m0, s22, s40
	v_and_b32_e32 v67, 0xffff0000, v0
	global_load_lds_dwordx4 v[230:231], off
	ds_read_b32 v64, v113
	ds_read_b32 v65, v145
	v_lshlrev_b32_e32 v68, 16, v1
	v_and_b32_e32 v69, 0xffff0000, v1
	v_lshlrev_b32_e32 v70, 16, v2
	s_waitcnt lgkmcnt(0)
	v_sub_f32_e32 v66, v66, v64
	v_mul_f32_e32 v66, v65, v66
	v_sub_f32_e32 v67, v67, v64
	v_mul_f32_e32 v67, v65, v67
	v_and_b32_e32 v71, 0xffff0000, v2
	v_lshlrev_b32_e32 v72, 16, v3
	v_and_b32_e32 v73, 0xffff0000, v3
	v_lshlrev_b32_e32 v74, 16, v7
	v_and_b32_e32 v75, 0xffff0000, v7
	v_lshlrev_b32_e32 v76, 16, v11
	v_and_b32_e32 v77, 0xffff0000, v11
	v_lshlrev_b32_e32 v78, 16, v15
	v_and_b32_e32 v79, 0xffff0000, v15
	s_cmpk_eq_i32 s6, 0xc00
	s_waitcnt vmcnt(8)
	s_branch .Lo2_after_wait

; __device__ __forceinline__ unsigned pk2(float lo, float hi) { unsigned r; asm("v_cvt_pk_bf16_f32 %0, %1, %2" : "=v"(r) : "v"(lo), "v"(hi)); return r; }
; __device__ __forceinline__ void phase_sgu(CArgs a, LAS unsigned char* lds, int i2, int wv, int xw  ) {
;     ...
;                 for (int it = 0; it < 8; ++it) { const int j = 32 * (it & 3) + (lane & 31), q = it >> 2, c8 = cA + 16 * q;
;                     const float m = mu[j], r = rs[j]; const u32x4 raw = vraw[it];
;                     const float v[8] = {bflo(raw.x), bfhi(raw.x), bflo(raw.y), bfhi(raw.y), bflo(raw.z), bfhi(raw.z), bflo(raw.w), bfhi(raw.w)};
; #pragma unroll
;                     for (int k = 0; k < 8; k += 2) { const unsigned pr = pk2((v[k] - m) * r * gg[q][k >> 2][k & 3] + bb[q][k >> 2][k & 3], (v[k + 1] - m) * r * gg[q][k >> 2][(k + 1) & 3] + bb[q][k >> 2][(k + 1) & 3]);
;                         vt[(c8 * 8 + k) * VS + j] = (bf16)(pr & 0xffffu); vt[(c8 * 8 + k + 1) * VS + j] = (bf16)(pr >> 16); } }
.Lo2_after_wait:
	v_fma_f32 v66, v56, v66, v60
	v_fma_f32 v67, v57, v67, v61
	v_cvt_pk_bf16_f32 v66, v66, v67
	ds_write_b16 v157, v66
	ds_write_b16_d16_hi v157, v66 offset:272
	v_sub_f32_e32 v66, v68, v64
	v_mul_f32_e32 v66, v65, v66
	v_sub_f32_e32 v67, v69, v64
	v_fma_f32 v66, v58, v66, v62
	v_mul_f32_e32 v67, v65, v67
	v_fma_f32 v67, v59, v67, v63
	v_cvt_pk_bf16_f32 v66, v66, v67
	ds_write_b16 v157, v66 offset:544
	ds_write_b16_d16_hi v157, v66 offset:816
	v_sub_f32_e32 v66, v70, v64
	v_mul_f32_e32 v66, v65, v66
	v_sub_f32_e32 v67, v71, v64
	v_fma_f32 v66, v48, v66, v52
	v_mul_f32_e32 v67, v65, v67
	v_fma_f32 v67, v49, v67, v53
	v_cvt_pk_bf16_f32 v66, v66, v67
	ds_write_b16 v157, v66 offset:1088
	ds_write_b16_d16_hi v157, v66 offset:1360
	v_sub_f32_e32 v66, v72, v64
	v_mul_f32_e32 v66, v65, v66
	v_sub_f32_e32 v67, v73, v64
	v_fma_f32 v66, v50, v66, v54
	v_mul_f32_e32 v67, v65, v67
	v_fma_f32 v67, v51, v67, v55
	v_cvt_pk_bf16_f32 v66, v66, v67
	ds_write_b16 v157, v66 offset:1632
	ds_write_b16_d16_hi v157, v66 offset:1904
	ds_read_b32 v66, v169
	ds_read_b32 v67, v176
	v_lshlrev_b32_e32 v68, 16, v4
	v_and_b32_e32 v69, 0xffff0000, v4
	v_lshlrev_b32_e32 v70, 16, v5
	s_waitcnt lgkmcnt(1)
	v_sub_f32_e32 v68, v68, v66
	s_waitcnt lgkmcnt(0)
	v_mul_f32_e32 v68, v67, v68
	v_sub_f32_e32 v69, v69, v66
	v_fma_f32 v68, v56, v68, v60
	v_mul_f32_e32 v69, v67, v69
	v_fma_f32 v69, v57, v69, v61
	v_cvt_pk_bf16_f32 v68, v68, v69
	v_and_b32_e32 v71, 0xffff0000, v5
	ds_write_b16 v157, v68 offset:64
	ds_write_b16_d16_hi v157, v68 offset:336
	v_sub_f32_e32 v68, v70, v66
	v_mul_f32_e32 v68, v67, v68
	v_sub_f32_e32 v69, v71, v66
	v_fma_f32 v68, v58, v68, v62
	v_mul_f32_e32 v69, v67, v69
	v_lshlrev_b32_e32 v72, 16, v6
	v_fma_f32 v69, v59, v69, v63
	v_cvt_pk_bf16_f32 v68, v68, v69
	v_and_b32_e32 v73, 0xffff0000, v6
	ds_write_b16 v157, v68 offset:608
	ds_write_b16_d16_hi v157, v68 offset:880
	v_sub_f32_e32 v68, v72, v66
	v_mul_f32_e32 v68, v67, v68
	v_sub_f32_e32 v69, v73, v66
	v_fma_f32 v68, v48, v68, v52
	v_mul_f32_e32 v69, v67, v69
	v_fma_f32 v69, v49, v69, v53
	v_cvt_pk_bf16_f32 v68, v68, v69
	ds_write_b16 v157, v68 offset:1152
	ds_write_b16_d16_hi v157, v68 offset:1424
	v_sub_f32_e32 v68, v74, v66
	v_mul_f32_e32 v68, v67, v68
	v_sub_f32_e32 v69, v75, v66
	v_fma_f32 v68, v50, v68, v54
	v_mul_f32_e32 v69, v67, v69
	v_fma_f32 v69, v51, v69, v55
	v_cvt_pk_bf16_f32 v68, v68, v69
	ds_write_b16 v157, v68 offset:1696
	ds_write_b16_d16_hi v157, v68 offset:1968
	ds_read_b32 v68, v177
	ds_read_b32 v69, v192
	v_lshlrev_b32_e32 v70, 16, v8
	v_and_b32_e32 v71, 0xffff0000, v8
	v_lshlrev_b32_e32 v72, 16, v9
	s_waitcnt lgkmcnt(1)
	v_sub_f32_e32 v70, v70, v68
	s_waitcnt lgkmcnt(0)
	v_mul_f32_e32 v70, v69, v70
	v_sub_f32_e32 v71, v71, v68
	v_fma_f32 v70, v56, v70, v60
	v_mul_f32_e32 v71, v69, v71
	v_fma_f32 v71, v57, v71, v61
	v_cvt_pk_bf16_f32 v70, v70, v71
	v_and_b32_e32 v73, 0xffff0000, v9
	ds_write_b16 v157, v70 offset:128
	ds_write_b16_d16_hi v157, v70 offset:400
	v_sub_f32_e32 v70, v72, v68
	v_mul_f32_e32 v70, v69, v70
	v_sub_f32_e32 v71, v73, v68
	v_fma_f32 v70, v58, v70, v62
	v_mul_f32_e32 v71, v69, v71
	v_lshlrev_b32_e32 v74, 16, v10
	v_fma_f32 v71, v59, v71, v63
	v_cvt_pk_bf16_f32 v70, v70, v71
	v_and_b32_e32 v75, 0xffff0000, v10
	ds_write_b16 v157, v70 offset:672
	ds_write_b16_d16_hi v157, v70 offset:944
	v_sub_f32_e32 v70, v74, v68
	v_mul_f32_e32 v70, v69, v70
	v_sub_f32_e32 v71, v75, v68
	v_fma_f32 v70, v48, v70, v52
	v_mul_f32_e32 v71, v69, v71
	v_fma_f32 v71, v49, v71, v53
	v_cvt_pk_bf16_f32 v70, v70, v71
	ds_write_b16 v157, v70 offset:1216
	ds_write_b16_d16_hi v157, v70 offset:1488
	v_sub_f32_e32 v70, v76, v68
	v_mul_f32_e32 v70, v69, v70
	v_sub_f32_e32 v71, v77, v68
	v_fma_f32 v70, v50, v70, v54
	v_mul_f32_e32 v71, v69, v71
	v_fma_f32 v71, v51, v71, v55
	v_cvt_pk_bf16_f32 v70, v70, v71
	ds_write_b16 v157, v70 offset:1760
	ds_write_b16_d16_hi v157, v70 offset:2032
	ds_read_b32 v70, v193
	ds_read_b32 v71, v194
	v_lshlrev_b32_e32 v72, 16, v12
	v_and_b32_e32 v73, 0xffff0000, v12
	v_lshlrev_b32_e32 v74, 16, v13
	s_waitcnt lgkmcnt(1)
	v_sub_f32_e32 v72, v72, v70
	s_waitcnt lgkmcnt(0)
	v_mul_f32_e32 v72, v71, v72
	v_fma_f32 v56, v56, v72, v60
	v_sub_f32_e32 v60, v73, v70
	v_mul_f32_e32 v60, v71, v60
	v_fma_f32 v57, v57, v60, v61
	v_cvt_pk_bf16_f32 v56, v56, v57
	v_and_b32_e32 v75, 0xffff0000, v13
	ds_write_b16 v157, v56 offset:192
	ds_write_b16_d16_hi v157, v56 offset:464
	v_sub_f32_e32 v56, v74, v70
	v_mul_f32_e32 v56, v71, v56
	v_sub_f32_e32 v57, v75, v70
	v_fma_f32 v56, v58, v56, v62
	v_mul_f32_e32 v57, v71, v57
	v_lshlrev_b32_e32 v76, 16, v14
	v_fmac_f32_e32 v63, v59, v57
	v_cvt_pk_bf16_f32 v56, v56, v63
	ds_write_b16 v157, v56 offset:736
	ds_write_b16_d16_hi v157, v56 offset:1008
	v_sub_f32_e32 v56, v76, v70
	v_and_b32_e32 v77, 0xffff0000, v14
	v_mul_f32_e32 v56, v71, v56
	v_fma_f32 v48, v48, v56, v52
	v_sub_f32_e32 v52, v77, v70
	v_mul_f32_e32 v52, v71, v52
	v_fma_f32 v49, v49, v52, v53
	v_cvt_pk_bf16_f32 v48, v48, v49
	ds_write_b16 v157, v48 offset:1280
	ds_write_b16_d16_hi v157, v48 offset:1552
	v_sub_f32_e32 v48, v78, v70
	v_mul_f32_e32 v48, v71, v48
	v_sub_f32_e32 v49, v79, v70
	v_fma_f32 v48, v50, v48, v54
	v_mul_f32_e32 v49, v71, v49
	v_fmac_f32_e32 v55, v51, v49
	v_cvt_pk_bf16_f32 v48, v48, v55
	ds_write_b16 v157, v48 offset:1824
	ds_write_b16_d16_hi v157, v48 offset:2096
	v_lshlrev_b32_e32 v48, 16, v16
	v_and_b32_e32 v49, 0xffff0000, v16
	v_sub_f32_e32 v48, v48, v64
	v_mul_f32_e32 v48, v65, v48
	v_sub_f32_e32 v49, v49, v64
	v_fma_f32 v48, v40, v48, v44
	v_mul_f32_e32 v49, v65, v49
	v_lshlrev_b32_e32 v50, 16, v17
	v_fma_f32 v49, v41, v49, v45
; __device__ __forceinline__ unsigned pk2(float lo, float hi) { unsigned r; asm("v_cvt_pk_bf16_f32 %0, %1, %2" : "=v"(r) : "v"(lo), "v"(hi)); return r; }
; __device__ __forceinline__ void phase_sgu(CArgs a, LAS unsigned char* lds, int i2, int wv, int xw  ) {
;     ...
;                 for (int it = 0; it < 8; ++it) { const int j = 32 * (it & 3) + (lane & 31), q = it >> 2, c8 = cA + 16 * q;
;                     const float m = mu[j], r = rs[j]; const u32x4 raw = vraw[it];
;                     const float v[8] = {bflo(raw.x), bfhi(raw.x), bflo(raw.y), bfhi(raw.y), bflo(raw.z), bfhi(raw.z), bflo(raw.w), bfhi(raw.w)};
; #pragma unroll
;                     for (int k = 0; k < 8; k += 2) { const unsigned pr = pk2((v[k] - m) * r * gg[q][k >> 2][k & 3] + bb[q][k >> 2][k & 3], (v[k + 1] - m) * r * gg[q][k >> 2][(k + 1) & 3] + bb[q][k >> 2][(k + 1) & 3]);
;                         vt[(c8 * 8 + k) * VS + j] = (bf16)(pr & 0xffffu); vt[(c8 * 8 + k + 1) * VS + j] = (bf16)(pr >> 16); } }
;             }
;             if (hh < 3) {
; #pragma unroll
;                 for (int it = 0; it < 8; ++it) { const int j = 32 * (it & 3) + (lane & 31), c8 = 2 * (8 * (it >> 2) + wave) + (lane >> 5);
;                     vraw[it] = *(const u32x4*)(HB + (tok0 + j) * (2 * SGU_W) + SGU_W + (h + 1) * 256 + c8 * 8); } }
	v_cvt_pk_bf16_f32 v48, v48, v49
	v_and_b32_e32 v51, 0xffff0000, v17
	ds_write_b16 v195, v48
	ds_write_b16_d16_hi v195, v48 offset:272
	v_sub_f32_e32 v48, v50, v64
	v_mul_f32_e32 v48, v65, v48
	v_sub_f32_e32 v49, v51, v64
	v_fma_f32 v48, v42, v48, v46
	v_mul_f32_e32 v49, v65, v49
	v_lshlrev_b32_e32 v52, 16, v18
	v_fma_f32 v49, v43, v49, v47
	v_cvt_pk_bf16_f32 v48, v48, v49
	v_and_b32_e32 v53, 0xffff0000, v18
	ds_write_b16 v157, v48 offset:35360
	ds_write_b16_d16_hi v157, v48 offset:35632
	v_sub_f32_e32 v48, v52, v64
	v_mul_f32_e32 v48, v65, v48
	v_sub_f32_e32 v49, v53, v64
	v_fma_f32 v48, v32, v48, v36
	v_mul_f32_e32 v49, v65, v49
	v_lshlrev_b32_e32 v54, 16, v19
	v_fma_f32 v49, v33, v49, v37
	v_cvt_pk_bf16_f32 v48, v48, v49
	v_and_b32_e32 v55, 0xffff0000, v19
	ds_write_b16 v157, v48 offset:35904
	ds_write_b16_d16_hi v157, v48 offset:36176
	v_sub_f32_e32 v48, v54, v64
	v_mul_f32_e32 v48, v65, v48
	v_sub_f32_e32 v49, v55, v64
	v_fma_f32 v48, v34, v48, v38
	v_mul_f32_e32 v49, v65, v49
	v_fma_f32 v49, v35, v49, v39
	v_cvt_pk_bf16_f32 v48, v48, v49
	ds_write_b16 v157, v48 offset:36448
	ds_write_b16_d16_hi v157, v48 offset:36720
	v_lshlrev_b32_e32 v48, 16, v20
	v_and_b32_e32 v49, 0xffff0000, v20
	v_sub_f32_e32 v48, v48, v66
	v_mul_f32_e32 v48, v67, v48
	v_sub_f32_e32 v49, v49, v66
	v_fma_f32 v48, v40, v48, v44
	v_mul_f32_e32 v49, v67, v49
	v_lshlrev_b32_e32 v50, 16, v21
	v_fma_f32 v49, v41, v49, v45
	v_cvt_pk_bf16_f32 v48, v48, v49
	v_and_b32_e32 v51, 0xffff0000, v21
	ds_write_b16 v195, v48 offset:64
	ds_write_b16_d16_hi v195, v48 offset:336
	v_sub_f32_e32 v48, v50, v66
	v_mul_f32_e32 v48, v67, v48
	v_sub_f32_e32 v49, v51, v66
	v_fma_f32 v48, v42, v48, v46
	v_mul_f32_e32 v49, v67, v49
	v_lshlrev_b32_e32 v52, 16, v22
	v_fma_f32 v49, v43, v49, v47
	v_cvt_pk_bf16_f32 v48, v48, v49
	v_and_b32_e32 v53, 0xffff0000, v22
	ds_write_b16 v157, v48 offset:35424
	ds_write_b16_d16_hi v157, v48 offset:35696
	v_sub_f32_e32 v48, v52, v66
	v_mul_f32_e32 v48, v67, v48
	v_sub_f32_e32 v49, v53, v66
	v_fma_f32 v48, v32, v48, v36
	v_mul_f32_e32 v49, v67, v49
	v_lshlrev_b32_e32 v54, 16, v23
	v_fma_f32 v49, v33, v49, v37
	v_cvt_pk_bf16_f32 v48, v48, v49
	v_and_b32_e32 v55, 0xffff0000, v23
	ds_write_b16 v157, v48 offset:35968
	ds_write_b16_d16_hi v157, v48 offset:36240
	v_sub_f32_e32 v48, v54, v66
	v_mul_f32_e32 v48, v67, v48
	v_sub_f32_e32 v49, v55, v66
	v_fma_f32 v48, v34, v48, v38
	v_mul_f32_e32 v49, v67, v49
	v_fma_f32 v49, v35, v49, v39
	v_cvt_pk_bf16_f32 v48, v48, v49
	ds_write_b16 v157, v48 offset:36512
	ds_write_b16_d16_hi v157, v48 offset:36784
	v_lshlrev_b32_e32 v48, 16, v24
	v_and_b32_e32 v49, 0xffff0000, v24
	v_sub_f32_e32 v48, v48, v68
	v_mul_f32_e32 v48, v69, v48
	v_sub_f32_e32 v49, v49, v68
	v_fma_f32 v48, v40, v48, v44
	v_mul_f32_e32 v49, v69, v49
	v_lshlrev_b32_e32 v50, 16, v25
	v_fma_f32 v49, v41, v49, v45
	v_cvt_pk_bf16_f32 v48, v48, v49
	v_and_b32_e32 v51, 0xffff0000, v25
	ds_write_b16 v195, v48 offset:128
	ds_write_b16_d16_hi v195, v48 offset:400
	v_sub_f32_e32 v48, v50, v68
	v_mul_f32_e32 v48, v69, v48
	v_sub_f32_e32 v49, v51, v68
	v_fma_f32 v48, v42, v48, v46
	v_mul_f32_e32 v49, v69, v49
	v_lshlrev_b32_e32 v52, 16, v26
	v_fma_f32 v49, v43, v49, v47
	v_cvt_pk_bf16_f32 v48, v48, v49
	v_and_b32_e32 v53, 0xffff0000, v26
	ds_write_b16 v157, v48 offset:35488
	ds_write_b16_d16_hi v157, v48 offset:35760
	v_sub_f32_e32 v48, v52, v68
	v_mul_f32_e32 v48, v69, v48
	v_sub_f32_e32 v49, v53, v68
	v_fma_f32 v48, v32, v48, v36
	v_mul_f32_e32 v49, v69, v49
	v_lshlrev_b32_e32 v54, 16, v27
	v_fma_f32 v49, v33, v49, v37
	v_cvt_pk_bf16_f32 v48, v48, v49
	v_and_b32_e32 v55, 0xffff0000, v27
	ds_write_b16 v157, v48 offset:36032
	ds_write_b16_d16_hi v157, v48 offset:36304
	v_sub_f32_e32 v48, v54, v68
	v_mul_f32_e32 v48, v69, v48
	v_sub_f32_e32 v49, v55, v68
	v_fma_f32 v48, v34, v48, v38
	v_mul_f32_e32 v49, v69, v49
	v_fma_f32 v49, v35, v49, v39
	v_cvt_pk_bf16_f32 v48, v48, v49
	ds_write_b16 v157, v48 offset:36576
	ds_write_b16_d16_hi v157, v48 offset:36848
	v_lshlrev_b32_e32 v48, 16, v28
	v_sub_f32_e32 v48, v48, v70
	v_and_b32_e32 v49, 0xffff0000, v28
	v_mul_f32_e32 v48, v71, v48
	v_fma_f32 v40, v40, v48, v44
	v_sub_f32_e32 v44, v49, v70
	v_mul_f32_e32 v44, v71, v44
	v_lshlrev_b32_e32 v50, 16, v29
	v_fma_f32 v41, v41, v44, v45
	v_cvt_pk_bf16_f32 v40, v40, v41
	v_and_b32_e32 v51, 0xffff0000, v29
	ds_write_b16 v195, v40 offset:192
	ds_write_b16_d16_hi v195, v40 offset:464
	v_sub_f32_e32 v40, v50, v70
	v_mul_f32_e32 v40, v71, v40
	v_sub_f32_e32 v41, v51, v70
	v_fma_f32 v40, v42, v40, v46
	v_mul_f32_e32 v41, v71, v41
	v_lshlrev_b32_e32 v52, 16, v30
	v_fmac_f32_e32 v47, v43, v41
	v_cvt_pk_bf16_f32 v40, v40, v47
	ds_write_b16 v157, v40 offset:35552
	ds_write_b16_d16_hi v157, v40 offset:35824
	v_sub_f32_e32 v40, v52, v70
	v_and_b32_e32 v53, 0xffff0000, v30
	v_mul_f32_e32 v40, v71, v40
	v_fma_f32 v32, v32, v40, v36
	v_sub_f32_e32 v36, v53, v70
	v_mul_f32_e32 v36, v71, v36
	v_lshlrev_b32_e32 v54, 16, v31
	v_fma_f32 v33, v33, v36, v37
	v_cvt_pk_bf16_f32 v32, v32, v33
	v_and_b32_e32 v55, 0xffff0000, v31
	ds_write_b16 v157, v32 offset:36096
	ds_write_b16_d16_hi v157, v32 offset:36368
	v_sub_f32_e32 v32, v54, v70
	v_mul_f32_e32 v32, v71, v32
	v_sub_f32_e32 v33, v55, v70
	v_fma_f32 v32, v34, v32, v38
	v_mul_f32_e32 v33, v71, v33
	v_fmac_f32_e32 v39, v35, v33
	v_cvt_pk_bf16_f32 v32, v32, v39
	ds_write_b16 v157, v32 offset:36640
	ds_write_b16_d16_hi v157, v32 offset:36912
	s_cbranch_scc1 .LBB0_283
	v_lshl_add_u64 v[8:9], s[4:5], 0, v[130:131]
	v_add_co_u32_e32 v0, vcc, 0x3a001000, v8
	v_lshl_add_u64 v[24:25], s[4:5], 0, v[128:129]
	s_nop 0
	v_addc_co_u32_e32 v1, vcc, 0, v9, vcc
	v_add_co_u32_e32 v4, vcc, 0x3a041000, v8
	s_mov_b32 s22, 0x3a001000
	s_nop 0
	v_addc_co_u32_e32 v5, vcc, 0, v9, vcc
	v_add_co_u32_e32 v10, vcc, 0x3a081000, v8
	global_load_dwordx4 v[0:3], v[0:1], off offset:512
	s_nop 0
	global_load_dwordx4 v[4:7], v[4:5], off offset:512
	v_addc_co_u32_e32 v11, vcc, 0, v9, vcc
	v_add_co_u32_e32 v12, vcc, 0x3a0c1000, v8
	s_nop 1
	v_addc_co_u32_e32 v13, vcc, 0, v9, vcc
	v_add_co_u32_e32 v16, vcc, s22, v24
	global_load_dwordx4 v[8:11], v[10:11], off offset:512
	s_nop 0
	global_load_dwordx4 v[12:15], v[12:13], off offset:512
	v_addc_co_u32_e32 v17, vcc, 0, v25, vcc
	v_add_co_u32_e32 v20, vcc, 0x3a041000, v24
	s_nop 1
	v_addc_co_u32_e32 v21, vcc, 0, v25, vcc
	v_add_co_u32_e32 v26, vcc, 0x3a081000, v24
	global_load_dwordx4 v[16:19], v[16:17], off offset:512
	s_nop 0
	global_load_dwordx4 v[20:23], v[20:21], off offset:512
	v_addc_co_u32_e32 v27, vcc, 0, v25, vcc
	v_add_co_u32_e32 v28, vcc, 0x3a0c1000, v24
	s_nop 1
	v_addc_co_u32_e32 v29, vcc, 0, v25, vcc
	global_load_dwordx4 v[24:27], v[26:27], off offset:512
	s_nop 0
	global_load_dwordx4 v[28:31], v[28:29], off offset:512
	s_branch .LBB0_283
